# C3: next item's prologue inputs (norm statistics, attention rows, V^T tile, q column) requested during the previous item's last direction step
# baseline (speedup 1.0000x reference)
; #define LAS __attribute__((address_space(3)))
; __device__ __forceinline__ int tid_hidden() { int t = threadIdx.x; asm volatile("" : "+v"(t)); return t; }
; #define lds lds_hidden(lds0)
; __device__ __forceinline__ void c3_phase(LAS unsigned char* lds, const bf16_t* __restrict__ QH, const bf16_t* __restrict__ LF, const bf16_t* __restrict__ VTH, const bf16_t* __restrict__ SIN, ...
;     const int tid = tid_hidden(), wid = __builtin_amdgcn_readfirstlane(tid >> 6), lane = tid & 63, l15 = lane & 15, g4 = lane >> 4;
;     const int d = tid & 127, tq = tid >> 7, tau = wid & 3, eh = wid >> 2;
;     LAS float* qtot = (LAS float*)(lds + C3_QTOT);
;     LAS float* red = (LAS float*)(lds + C3_RED);
;     unsigned lfn[16]; u32x4 stn[4];
;     ...
;     if (c < NB * 4 * 32) C3_PREFETCH(c, 0);
.LBB0_1091:
	s_andn2_b64 vcc, exec, s[0:1]
	s_cbranch_vccnz .LBB0_1175
	s_mov_b32 s14, s91
	s_mov_b64 s[0:1], s[86:87]
	s_load_dwordx2 s[0:1], s[0:1], 0xa8
	s_mov_b64 s[2:3], s[86:87]
	s_mov_b64 s[4:5], s[86:87]
	s_mov_b64 s[6:7], s[86:87]
	s_mov_b64 s[8:9], s[86:87]
	s_waitcnt lgkmcnt(0)
	s_add_u32 s0, s0, 0xb808000
	s_addc_u32 s1, s1, 0
	s_load_dwordx2 s[2:3], s[2:3], 0xa8
	s_mov_b64 s[12:13], s[86:87]
	s_waitcnt vmcnt(0)
	v_mov_b32_e32 v18, v0
	s_movk_i32 s26, 0x6000
	s_movk_i32 s25, 0x4000
	s_waitcnt lgkmcnt(0)
	s_add_u32 s2, s2, 0xc808000
	s_addc_u32 s3, s3, 0
	s_load_dwordx2 s[4:5], s[4:5], 0xa8
	s_movk_i32 s24, 0x2000
	s_waitcnt lgkmcnt(0)
	s_add_u32 s4, s4, 0x10808000
	s_addc_u32 s5, s5, 0
	s_load_dwordx2 s[6:7], s[6:7], 0xa8
	s_waitcnt lgkmcnt(0)
	s_add_u32 s10, s6, 0x17888000
	s_addc_u32 s11, s7, 0
	s_load_dwordx2 s[8:9], s[8:9], 0xa8
	s_mov_b64 s[6:7], s[86:87]
	s_waitcnt lgkmcnt(0)
	s_add_u32 s8, s8, 0x11808000
	s_addc_u32 s9, s9, 0
	s_nop 0
	v_writelane_b32 v254, s8, 14
	s_nop 1
	v_writelane_b32 v254, s9, 15
	s_load_dwordx2 s[8:9], s[12:13], 0xa8
	s_mov_b64 s[12:13], s[86:87]
	s_waitcnt lgkmcnt(0)
	s_add_u32 s8, s8, 0x12808000
	s_addc_u32 s9, s9, 0
	s_load_dwordx2 s[12:13], s[12:13], 0xa8
	v_writelane_b32 v254, s8, 16
	s_waitcnt lgkmcnt(0)
	s_add_u32 s12, s12, 0x13808000
	s_addc_u32 s13, s13, 0
	v_writelane_b32 v254, s9, 17
	s_mov_b64 s[8:9], s[86:87]
	v_writelane_b32 v254, s12, 18
	s_nop 1
	v_writelane_b32 v254, s13, 19
	s_load_dwordx2 s[12:13], s[86:87], 0xa8
	v_readlane_b32 s82, v254, 0
	s_waitcnt lgkmcnt(0)
	s_add_u32 s86, s12, 0x6008000
	s_addc_u32 s87, s13, 0
	s_load_dword s12, s[78:79], 0x0
	s_waitcnt lgkmcnt(0)
	s_cmpk_gt_i32 s82, 0x3ff
	v_readfirstlane_b32 s15, v18
	v_writelane_b32 v254, s12, 20
	s_cbranch_scc1 .LBB0_1113
	s_load_dwordx2 s[8:9], s[8:9], 0x40
	s_nop 0
	s_load_dwordx2 s[12:13], s[6:7], 0x50
	v_readlane_b32 s6, v254, 12
	v_readlane_b32 s7, v254, 13
	s_lshl_b32 s90, s6, 9
	s_mov_b32 s16, s6
	s_lshl_b64 s[6:7], s[90:91], 2
	s_waitcnt lgkmcnt(0)
	s_add_u32 s6, s8, s6
	s_addc_u32 s7, s9, s7
	s_lshl_b32 s90, s16, 7
	s_lshl_b64 s[8:9], s[90:91], 2
	s_add_u32 s12, s12, s8
	s_addc_u32 s13, s13, s9
	s_ashr_i32 s8, s82, 7
	v_ashrrev_i32_e32 v19, 7, v18
	s_and_b32 s22, s82, 31
	s_ashr_i32 s9, s8, 31
	s_lshl_b64 s[16:17], s[8:9], 11
	s_lshl_b32 s23, s22, 6
	v_lshlrev_b32_e32 v52, 4, v19
	s_ashr_i32 s20, s15, 6
	s_bfe_u32 s21, s82, 0x20005
	s_or_b32 s16, s16, s23
	v_ashrrev_i32_e32 v53, 31, v52
	s_add_i32 s18, s14, 0x1a400
	s_add_i32 s19, s14, 0x19c00
	s_and_b32 s46, s20, 3
	s_lshl_b32 s23, s21, 5
	v_lshl_add_u64 v[2:3], s[16:17], 0, v[52:53]
	s_lshl_b32 s16, s21, 8
	v_and_b32_e32 v36, 0x7f, v18
	s_add_u32 s16, s2, s16
	s_addc_u32 s17, s3, 0
	v_lshlrev_b32_e32 v34, 1, v36
	v_lshl_add_u64 v[4:5], s[16:17], 0, v[34:35]
	v_lshlrev_b64 v[2:3], 11, v[2:3]
	v_lshl_add_u64 v[2:3], v[4:5], 0, v[2:3]
	s_movk_i32 s16, 0x1000
	v_add_co_u32_e32 v4, vcc, s16, v2
	s_movk_i32 s16, 0x3000
	s_nop 0
	v_addc_co_u32_e32 v5, vcc, 0, v3, vcc
	v_add_co_u32_e32 v6, vcc, s24, v2
	s_lshl_b64 s[8:9], s[8:9], 7
	s_nop 0
	v_addc_co_u32_e32 v7, vcc, 0, v3, vcc
	v_add_co_u32_e32 v8, vcc, s16, v2
	s_movk_i32 s16, 0x5000
	s_nop 0
	v_addc_co_u32_e32 v9, vcc, 0, v3, vcc
	v_add_co_u32_e32 v10, vcc, s25, v2
	s_or_b32 s8, s8, s23
	s_nop 0
	v_addc_co_u32_e32 v11, vcc, 0, v3, vcc
	v_add_co_u32_e32 v12, vcc, s16, v2
	s_movk_i32 s16, 0x7000
	s_nop 0
	v_addc_co_u32_e32 v13, vcc, 0, v3, vcc
	v_add_co_u32_e32 v14, vcc, s26, v2
	s_or_b32 s8, s8, s22
	s_nop 0
	v_addc_co_u32_e32 v15, vcc, 0, v3, vcc
	v_mov_b32_e32 v255, 0
	global_load_ushort v65, v[6:7], off offset:-4096
	global_load_ushort v160, v[6:7], off
	global_load_ushort v161, v[6:7], off offset:2048
	global_load_ushort v163, v[10:11], off offset:-4096
	global_load_ushort v165, v[10:11], off
	global_load_ushort v167, v[10:11], off offset:2048
	global_load_ushort v168, v[14:15], off offset:-4096
	global_load_ushort v170, v[14:15], off
	global_load_ushort v171, v[14:15], off offset:2048
	v_add_co_u32_e32 v6, vcc, s16, v2
	s_lshl_b64 s[8:9], s[8:9], 15
	s_nop 0
	v_addc_co_u32_e32 v7, vcc, 0, v3, vcc
	global_load_ushort v162, v[2:3], off
	global_load_ushort v164, v[2:3], off offset:2048
	global_load_ushort v166, v[4:5], off offset:2048
	global_load_ushort v169, v[8:9], off offset:2048
	global_load_ushort v172, v[12:13], off offset:2048
	global_load_ushort v173, v[6:7], off
	global_load_ushort v174, v[6:7], off offset:2048
	v_lshlrev_b32_e32 v2, 3, v18
	s_add_u32 s8, s10, s8
	v_lshlrev_b32_e32 v30, 4, v18
	v_and_b32_e32 v22, 0xffffff80, v2
	s_addc_u32 s9, s11, s9
	v_and_b32_e32 v20, 0xf0, v30
	v_mov_b32_e32 v21, v35
	v_add_u32_e32 v24, 0x1000, v22
	v_add_u32_e32 v26, 0x2000, v22
	v_add_u32_e32 v28, 0x3000, v22
	v_lshl_add_u64 v[10:11], s[8:9], 0, v[20:21]
	v_ashrrev_i32_e32 v23, 31, v22
	v_ashrrev_i32_e32 v25, 31, v24
	v_ashrrev_i32_e32 v27, 31, v26
	v_ashrrev_i32_e32 v29, 31, v28
	v_lshl_add_u64 v[2:3], v[22:23], 1, v[10:11]
	v_lshl_add_u64 v[6:7], v[24:25], 1, v[10:11]
	v_lshl_add_u64 v[12:13], v[26:27], 1, v[10:11]
	v_lshl_add_u64 v[14:15], v[28:29], 1, v[10:11]
	global_load_dwordx4 v[2:5], v[2:3], off nt
	s_nop 0
	global_load_dwordx4 v[6:9], v[6:7], off nt
	s_nop 0
	global_load_dwordx4 v[10:13], v[12:13], off nt
	s_nop 0
	global_load_dwordx4 v[14:17], v[14:15], off nt
	v_and_b32_e32 v30, 0x70, v30
	v_bfe_u32 v38, v18, 4, 2
	v_and_b32_e32 v39, 15, v18
	v_lshlrev_b32_e32 v32, 2, v30
	v_mov_b32_e32 v33, v35
	v_lshl_add_u64 v[56:57], s[6:7], 0, v[32:33]
	v_lshl_add_u64 v[60:61], s[0:1], 0, v[34:35]
	s_add_i32 s0, s14, 0x11400
	v_add_u32_e32 v33, s14, v34
	v_lshl_add_u64 v[62:63], s[2:3], 0, v[34:35]
; #define LAS __attribute__((address_space(3)))
; #define lds lds_hidden(lds0)
; __device__ __forceinline__ void c3_phase(LAS unsigned char* lds, const bf16_t* __restrict__ QH, const bf16_t* __restrict__ LF, const bf16_t* __restrict__ VTH, const bf16_t* __restrict__ SIN, ...
;     ...
;     const int d = tid & 127, tq = tid >> 7, tau = wid & 3, eh = wid >> 2;
;     LAS float* qtot = (LAS float*)(lds + C3_QTOT);
;     LAS float* red = (LAS float*)(lds + C3_RED);
;     unsigned lfn[16]; u32x4 stn[4];
;     ...
;     if (c < NB * 4 * 32) C3_PREFETCH(c, 0);
;     ...
;                     for (int r = 0; r < 4; ++r) { const int sp = sg * 16 + 4 * g4 + r, tp = tau * 16 + l15; const bool ok = dir == 0 ? (sp <= tp) : (sp >= tp); a[r] = ok ? a[r] : 0.f; }
	v_lshl_or_b32 v64, s46, 4, v39
	v_mov_b32_e32 v34, s14
	s_movk_i32 s76, 0x110
	v_lshlrev_b32_e32 v41, 4, v38
	v_add_u32_e32 v32, s0, v20
	v_lshl_add_u32 v176, v36, 2, s19
	v_mad_u32_u24 v36, v64, s76, v34
	v_lshlrev_b32_e32 v34, 2, v38
	v_add_u32_e32 v45, s0, v41
	s_lshl_b32 s0, s20, 4
	v_lshl_add_u64 v[66:67], s[10:11], 0, v[20:21]
	v_bitop3_b32 v20, s0, 64, v39 bitop3:0x36
	v_or_b32_e32 v49, 1, v34
	v_lshl_add_u32 v40, v39, 2, s18
	v_lshl_add_u32 v175, v18, 2, s19
	s_ashr_i32 s1, s15, 2
	v_cmp_eq_u32_e64 s[2:3], 0, v38
	v_lshl_add_u32 v177, v20, 2, s18
	v_cmp_ge_u32_e64 s[18:19], v49, v64
	v_or_b32_e32 v49, 2, v34
	s_andn2_b32 s1, s1, 63
	v_writelane_b32 v254, s2, 21
	v_cmp_le_u32_e64 s[20:21], v49, v64
	v_cmp_ge_u32_e64 s[22:23], v49, v64
	v_or_b32_e32 v49, 3, v34
	v_writelane_b32 v254, s3, 22
	s_and_b32 s2, s15, 0xffffffc0
	v_or_b32_e32 v20, s1, v34
	v_cmp_le_u32_e64 s[24:25], v49, v64
	v_cmp_ge_u32_e64 s[26:27], v49, v64
	v_or_b32_e32 v49, 16, v34
	v_mov_b32_e32 v31, v35
	v_ashrrev_i32_e32 v21, 31, v20
	s_movk_i32 s0, 0x1100
	s_cmp_eq_u32 s46, 0
	v_cmp_le_u32_e64 s[28:29], v49, v64
	v_cmp_ge_u32_e64 s[30:31], v49, v64
	v_or_b32_e32 v49, 17, v34
	v_lshl_add_u64 v[58:59], s[4:5], 0, v[30:31]
	v_cmp_lt_i32_e64 s[4:5], 0, v19
	v_cmp_lt_i32_e64 s[6:7], 1, v19
	v_cmp_lt_i32_e64 s[8:9], 2, v19
	v_or_b32_e32 v43, s1, v39
	v_lshl_add_u64 v[68:69], v[20:21], 2, s[12:13]
	v_mul_lo_u32 v19, v19, s0
	s_cselect_b64 s[12:13], -1, 0
	v_cmp_le_u32_e64 s[0:1], v34, v64
	s_cmp_lg_u32 s46, 0
	v_cmp_le_u32_e64 s[34:35], v49, v64
	v_cmp_ge_u32_e64 s[36:37], v49, v64
	v_or_b32_e32 v49, 18, v34
	v_writelane_b32 v254, s0, 23
	s_cselect_b64 s[94:95], -1, 0
	s_cmp_lt_u32 s46, 2
	v_cmp_le_u32_e64 s[38:39], v49, v64
	v_cmp_ge_u32_e64 s[40:41], v49, v64
	v_or_b32_e32 v49, 19, v34
	v_writelane_b32 v254, s1, 24
	s_cselect_b64 s[0:1], -1, 0
	v_cmp_le_u32_e64 s[42:43], v49, v64
	v_cmp_ge_u32_e64 s[44:45], v49, v64
	s_cmp_gt_u32 s46, 1
	v_or_b32_e32 v49, 32, v34
	s_cselect_b64 s[10:11], -1, 0
	s_cmp_lg_u32 s46, 3
	v_cmp_le_u32_e64 s[46:47], v49, v64
	v_cmp_ge_u32_e64 s[48:49], v49, v64
	v_or_b32_e32 v49, 33, v34
	v_cmp_le_u32_e64 s[50:51], v49, v64
	v_cmp_ge_u32_e64 s[52:53], v49, v64
	v_or_b32_e32 v49, 34, v34
	v_cmp_le_u32_e64 s[54:55], v49, v64
	v_cmp_ge_u32_e64 s[56:57], v49, v64
	v_or_b32_e32 v49, 35, v34
	v_cmp_le_u32_e64 s[58:59], v49, v64
	v_cmp_ge_u32_e64 s[60:61], v49, v64
	v_or_b32_e32 v49, 48, v34
	v_lshrrev_b32_e32 v37, 4, v18
	v_ashrrev_i32_e32 v54, 3, v18
	v_add_u32_e32 v46, 0x200, v18
	v_add_u32_e32 v48, 0x400, v18
	v_add_u32_e32 v18, 0x600, v18
	v_cmp_le_u32_e64 s[62:63], v49, v64
	v_cmp_ge_u32_e64 s[64:65], v49, v64
	v_or_b32_e32 v49, 49, v34
	s_movk_i32 s3, 0x90
	v_ashrrev_i32_e32 v70, 3, v46
	v_lshrrev_b32_e32 v46, 4, v46
	v_lshrrev_b32_e32 v48, 4, v48
	v_lshrrev_b32_e32 v18, 4, v18
	v_cmp_le_u32_e64 s[66:67], v49, v64
	v_cmp_ge_u32_e64 s[68:69], v49, v64
	v_or_b32_e32 v49, 50, v34
	v_add_u32_e32 v31, s14, v30
	v_add_u32_e32 v42, s14, v41
	v_lshl_add_u32 v44, v38, 3, s14
	v_mul_lo_u32 v38, v54, s3
	v_mul_lo_u32 v47, v70, s3
	v_mul_lo_u32 v37, v37, s76
	v_mul_lo_u32 v46, v46, s76
	v_mul_lo_u32 v48, v48, s76
	v_mul_lo_u32 v18, v18, s76
	v_mul_u32_u24_e32 v39, 0x110, v39
	v_cmp_le_u32_e64 s[70:71], v49, v64
	v_cmp_ge_u32_e64 s[72:73], v49, v64
	v_or_b32_e32 v49, 51, v34
	v_add_u32_e32 v178, s2, v40
	v_mul_lo_u32 v40, v43, s3
	v_mul_lo_u32 v43, v43, s76
	v_ashrrev_i32_e32 v55, 31, v54
	v_ashrrev_i32_e32 v71, 31, v70
	v_cmp_ge_u32_e64 s[14:15], v34, v64
	v_cmp_lt_u32_e64 s[16:17], v34, v64
	s_cselect_b64 s[96:97], -1, 0
	v_cmp_le_u32_e64 s[74:75], v49, v64
	v_lshlrev_b32_e32 v34, 1, v30
	v_add_u32_e32 v179, v31, v38
	v_add_u32_e32 v180, v31, v47
	v_lshlrev_b64 v[72:73], 1, v[22:23]
	v_lshlrev_b64 v[74:75], 1, v[24:25]
	v_lshlrev_b64 v[76:77], 1, v[26:27]
	v_lshlrev_b64 v[78:79], 1, v[28:29]
	v_add_u32_e32 v181, v32, v37
	v_add_u32_e32 v182, v32, v46
	v_add_u32_e32 v183, v32, v48
	v_add_u32_e32 v184, v32, v18
	v_add_u32_e32 v185, v33, v19
	v_add_u32_e32 v186, v44, v40
	v_add_u32_e32 v187, v45, v43
	v_lshlrev_b64 v[80:81], 1, v[20:21]
	v_add_u32_e32 v188, v36, v41
	v_add_u32_e32 v189, v42, v39
	v_cmp_ge_u32_e64 s[76:77], v49, v64
	v_writelane_b32 v254, s86, 25
	s_nop 1
	v_writelane_b32 v254, s87, 26
	s_branch .LBB0_1095
; __device__ __forceinline__ float kf(float x) { asm volatile("" : "+s"(x)); return x; }
; __device__ __forceinline__ void c3_phase(LAS unsigned char* lds, const bf16_t* __restrict__ QH, const bf16_t* __restrict__ LF, const bf16_t* __restrict__ VTH, const bf16_t* __restrict__ SIN, ...
;     ...
;     for (int item = c; item < NB * 4 * 32; item += G) {
;         const int b = item >> 7, h = (item >> 5) & 3, j = item & 31;
;         const size_t tok0 = (size_t)b * SEQ + j * 64;
;         { const int t = tid >> 3, c16 = (tid & 7) * 16; const size_t tok = tok0 + t;
;           const f32x4 s0 = *(const f32x4*)(SSQ + tok * 8), s1 = *(const f32x4*)(SSQ + tok * 8 + 4);
;           const float r = rsqrtf(((s0[0] + s0[1]) + (s0[2] + s0[3]) + (s1[0] + s1[1]) + (s1[2] + s1[3])) * (1.f / 512) + kf(EPS));
; #pragma unroll
;           for (int k = 0; k < 2; ++k) {
;               const u32x4 a = *(const u32x4*)(AO + tok * 512 + h * 128 + c16 + k * 8);
;               const f32x4 g0 = *(const f32x4*)(attn_gain + h * 128 + c16 + k * 8), g1 = *(const f32x4*)(attn_gain + h * 128 + c16 + k * 8 + 4);
;               u32x4 o;
;               o.x = cvt_pk_bf16(__uint_as_float(a.x << 16) * r * g0[0], __uint_as_float(a.x & 0xffff0000u) * r * g0[1]);
;     ...
;         float ss = 0.f;
; #pragma unroll
;         for (int et = 0; et < 4; ++et) ss += o[et][0] * o[et][0] + o[et][1] * o[et][1] + o[et][2] * o[et][2] + o[et][3] * o[et][3];
;         ss += shx(ss, 16); ss += shx(ss, 32);
;         if (g4 == 0) red[wid * 16 + l15] = ss;
;         __syncthreads();
;         const float tot = red[wid * 16 + l15] + red[(wid ^ 4) * 16 + l15];
;         const float rr = rsqrtf(tot * (1.f / 128) + kf(EPS));
;         const size_t tok = tok0 + tau * 16 + l15;
; #pragma unroll
;         for (int et = 0; et < 4; ++et) {
;             const int e0 = (eh * 4 + et) * 16 + 4 * g4;
;             const f32x4 gn = *(const f32x4*)(hg_gain + e0);
;             const u32x2 gv = *(const u32x2*)(GS + tok * 512 + h * 128 + e0);
;             u32x2 w;
;             w.x = cvt_pk_bf16(o[et][0] * rr * gn[0] * __uint_as_float(gv.x << 16), o[et][1] * rr * gn[1] * __uint_as_float(gv.x & 0xffff0000u));
;             w.y = cvt_pk_bf16(o[et][2] * rr * gn[2] * __uint_as_float(gv.y << 16), o[et][3] * rr * gn[3] * __uint_as_float(gv.y & 0xffff0000u));
;             *(u32x2*)(MIX + tok * D + 512 + h * 128 + e0) = w;
;         }
.LBB0_1094:
	s_or_b64 exec, exec, s[2:3]
	v_readlane_b32 s78, v254, 28
	v_readlane_b32 s79, v254, 29
	v_readlane_b32 s3, v254, 27
	v_or_b32_e32 v82, s78, v64
	v_mov_b32_e32 v83, s79
	v_readlane_b32 s78, v254, 14
	v_lshlrev_b64 v[40:41], 10, v[82:83]
	v_readlane_b32 s79, v254, 15
	s_mov_b32 s91, s81
	s_lshl_b32 s90, s3, 1
	v_lshl_add_u64 v[48:49], s[78:79], 0, v[40:41]
	s_mov_b32 s2, 0x358637bd
	v_lshl_add_u64 v[84:85], v[48:49], 0, s[90:91]
	s_waitcnt lgkmcnt(0)
	s_barrier
	ds_read_b32 v92, v178
	ds_read_b32 v93, v177
	v_lshl_add_u64 v[84:85], v[84:85], 0, v[80:81]
	v_mov_b32_e32 v94, s2
	s_waitcnt lgkmcnt(0)
	v_add_f32_e32 v92, v92, v93
	v_fmac_f32_e32 v94, 0x3c000000, v92
	s_mov_b32 s2, 0x800000
	v_mul_f32_e32 v92, 0x4b800000, v94
	v_cmp_gt_f32_e64 s[80:81], s2, v94
	v_readlane_b32 s86, v254, 25
	v_lshlrev_b64 v[82:83], 11, v[82:83]
	v_cndmask_b32_e64 v92, v94, v92, s[80:81]
	v_rsq_f32_e32 v92, v92
	v_readlane_b32 s87, v254, 26
	v_readlane_b32 s2, v254, 30
	v_readlane_b32 s3, v254, 31
	v_mul_f32_e32 v93, 0x45800000, v92
	v_cndmask_b32_e64 v92, v92, v93, s[80:81]
	v_pk_mul_f32 v[18:19], v[18:19], v[92:93] op_sel_hi:[1,0]
	v_pk_mul_f32 v[20:21], v[20:21], v[92:93] op_sel_hi:[1,0]
	v_lshl_add_u64 v[82:83], s[86:87], 0, v[82:83]
	v_pk_mul_f32 v[26:27], v[26:27], v[92:93] op_sel_hi:[1,0]
	v_pk_mul_f32 v[28:29], v[28:29], v[92:93] op_sel_hi:[1,0]
	v_pk_mul_f32 v[22:23], v[22:23], v[92:93] op_sel_hi:[1,0]
	v_pk_mul_f32 v[24:25], v[24:25], v[92:93] op_sel_hi:[1,0]
	v_pk_mul_f32 v[30:31], v[30:31], v[92:93] op_sel_hi:[1,0]
	v_pk_mul_f32 v[32:33], v[32:33], v[92:93] op_sel_hi:[1,0]
	v_lshl_add_u64 v[82:83], v[82:83], 0, s[90:91]
	s_andn2_b64 vcc, exec, s[2:3]
	v_lshl_add_u64 v[82:83], v[82:83], 0, v[80:81]
	s_mov_b32 s80, 0x800000
	s_waitcnt vmcnt(7)
	v_pk_mul_f32 v[18:19], v[96:97], v[18:19]
	v_pk_mul_f32 v[20:21], v[98:99], v[20:21]
	s_waitcnt vmcnt(3)
	v_lshlrev_b32_e32 v36, 16, v112
	v_and_b32_e32 v37, 0xffff0000, v112
	v_lshlrev_b32_e32 v38, 16, v113
	v_and_b32_e32 v39, 0xffff0000, v113
	v_pk_mul_f32 v[26:27], v[100:101], v[26:27]
	v_pk_mul_f32 v[28:29], v[102:103], v[28:29]
	v_pk_mul_f32 v[22:23], v[22:23], v[104:105]
	v_pk_mul_f32 v[24:25], v[24:25], v[106:107]
	v_pk_mul_f32 v[30:31], v[30:31], v[108:109]
	v_pk_mul_f32 v[32:33], v[32:33], v[110:111]
	s_waitcnt vmcnt(2)
	v_lshlrev_b32_e32 v40, 16, v114
	v_and_b32_e32 v41, 0xffff0000, v114
	v_lshlrev_b32_e32 v42, 16, v115
	v_and_b32_e32 v43, 0xffff0000, v115
	s_waitcnt vmcnt(1)
	v_lshlrev_b32_e32 v44, 16, v116
	v_and_b32_e32 v45, 0xffff0000, v116
	v_lshlrev_b32_e32 v46, 16, v117
	v_and_b32_e32 v47, 0xffff0000, v117
	s_waitcnt vmcnt(0)
	v_lshlrev_b32_e32 v48, 16, v118
	v_and_b32_e32 v49, 0xffff0000, v118
	v_lshlrev_b32_e32 v50, 16, v119
	v_and_b32_e32 v51, 0xffff0000, v119
	v_pk_mul_f32 v[18:19], v[18:19], v[36:37]
	v_pk_mul_f32 v[20:21], v[20:21], v[38:39]
	v_pk_mul_f32 v[26:27], v[26:27], v[40:41]
	v_pk_mul_f32 v[28:29], v[28:29], v[42:43]
	v_pk_mul_f32 v[22:23], v[22:23], v[44:45]
	v_pk_mul_f32 v[24:25], v[24:25], v[46:47]
	v_pk_mul_f32 v[30:31], v[30:31], v[48:49]
	v_pk_mul_f32 v[32:33], v[32:33], v[50:51]
	v_cvt_pk_bf16_f32 v18, v18, v19
	v_cvt_pk_bf16_f32 v19, v20, v21
	v_cvt_pk_bf16_f32 v20, v26, v27
	v_cvt_pk_bf16_f32 v21, v28, v29
	v_cvt_pk_bf16_f32 v22, v22, v23
	v_cvt_pk_bf16_f32 v23, v24, v25
	v_cvt_pk_bf16_f32 v24, v30, v31
	v_cvt_pk_bf16_f32 v25, v32, v33
	global_store_dwordx2 v[82:83], v[18:19], off offset:1024
	global_store_dwordx2 v[82:83], v[20:21], off offset:1056
	global_store_dwordx2 v[82:83], v[22:23], off offset:1088
	global_store_dwordx2 v[82:83], v[24:25], off offset:1120
	s_cbranch_vccz .LBB0_1113
.LBB0_1095:
	s_ashr_i32 s2, s82, 7
	s_and_b32 s78, s82, 31
	s_ashr_i32 s3, s2, 31
	s_mov_b32 s89, s82
	s_lshl_b64 s[82:83], s[2:3], 11
	s_lshl_b32 s79, s78, 6
	s_or_b32 s82, s82, s79
	v_lshl_add_u64 v[82:83], s[82:83], 0, v[54:55]
	v_readlane_b32 s84, v254, 18
	v_lshlrev_b64 v[18:19], 5, v[82:83]
	v_readlane_b32 s85, v254, 19
	s_mov_b64 s[80:81], s[86:87]
	v_readlane_b32 s86, v254, 16
	v_lshl_add_u64 v[22:23], s[84:85], 0, v[18:19]
	s_bfe_u32 s79, s89, 0x20005
	v_lshlrev_b64 v[26:27], 10, v[82:83]
	v_readlane_b32 s87, v254, 17
	s_lshl_b32 s90, s79, 8
	s_mov_b32 s84, 0x358637bd
	v_lshl_add_u64 v[26:27], s[86:87], 0, v[26:27]
	v_lshl_add_u64 v[26:27], v[26:27], 0, s[90:91]
	v_lshl_add_u64 v[30:31], v[26:27], 0, v[34:35]
	s_mov_b32 s87, s91
	s_lshl_b32 s86, s79, 9
	v_lshl_add_u64 v[48:49], v[56:57], 0, s[86:87]
	global_load_dwordx4 v[36:39], v[48:49], off
	global_load_dwordx4 v[40:43], v[48:49], off offset:16
	global_load_dwordx4 v[44:47], v[48:49], off offset:32
	s_nop 0
	global_load_dwordx4 v[48:51], v[48:49], off offset:48
	v_mov_b32_e32 v90, s84
	s_mov_b32 s85, 0x800000
	s_lshl_b32 vcc_lo, s79, 7
	s_lshl_b64 s[92:93], s[2:3], 9
	v_writelane_b32 v254, vcc_lo, 27
	s_or_b32 s92, s92, vcc_lo
	v_lshlrev_b64 v[82:83], 11, v[82:83]
	v_lshl_add_u64 v[82:83], s[80:81], 0, v[82:83]
	v_lshl_add_u64 v[82:83], v[82:83], 0, s[90:91]
	v_lshl_add_u64 v[82:83], v[82:83], 0, v[34:35]
	s_lshl_b32 s86, s78, 7
	v_lshl_add_u64 v[86:87], s[92:93], 0, v[54:55]
	v_writelane_b32 v254, s82, 28
	v_lshl_add_u64 v[84:85], v[58:59], 0, s[86:87]
	v_lshlrev_b64 v[86:87], 12, v[86:87]
	v_lshl_add_u64 v[86:87], v[84:85], 0, v[86:87]
	v_writelane_b32 v254, s83, 29
	v_readfirstlane_b32 vcc_lo, v255
	v_mov_b32_e32 v255, 0
	s_cmp_lg_u32 vcc_lo, 0
	s_cbranch_scc1 .Lc3_havepf
; #define LAS __attribute__((address_space(3)))
; __device__ __forceinline__ unsigned cvt_pk_bf16(float lo, float hi) { const bf16x2_t r = __builtin_convertvector((f32x2_t){lo, hi}, bf16x2_t); return __builtin_bit_cast(unsigned, r); }
; __device__ __forceinline__ float bf2f(bf16_t b) { return __uint_as_float(((unsigned)b) << 16); }
; __device__ __forceinline__ float kf(float x) { asm volatile("" : "+s"(x)); return x; }
; __device__ __forceinline__ void c3_phase(LAS unsigned char* lds, const bf16_t* __restrict__ QH, const bf16_t* __restrict__ LF, const bf16_t* __restrict__ VTH, const bf16_t* __restrict__ SIN, ...
;     ...
;         { const int t = tid >> 3, c16 = (tid & 7) * 16; const size_t tok = tok0 + t;
;           const f32x4 s0 = *(const f32x4*)(SSQ + tok * 8), s1 = *(const f32x4*)(SSQ + tok * 8 + 4);
;           const float r = rsqrtf(((s0[0] + s0[1]) + (s0[2] + s0[3]) + (s1[0] + s1[1]) + (s1[2] + s1[3])) * (1.f / 512) + kf(EPS));
; #pragma unroll
;           for (int k = 0; k < 2; ++k) {
;               const u32x4 a = *(const u32x4*)(AO + tok * 512 + h * 128 + c16 + k * 8);
;               const f32x4 g0 = *(const f32x4*)(attn_gain + h * 128 + c16 + k * 8), g1 = *(const f32x4*)(attn_gain + h * 128 + c16 + k * 8 + 4);
;               u32x4 o;
;               o.x = cvt_pk_bf16(__uint_as_float(a.x << 16) * r * g0[0], __uint_as_float(a.x & 0xffff0000u) * r * g0[1]);
;               o.y = cvt_pk_bf16(__uint_as_float(a.y << 16) * r * g0[2], __uint_as_float(a.y & 0xffff0000u) * r * g0[3]);
;               o.z = cvt_pk_bf16(__uint_as_float(a.z << 16) * r * g1[0], __uint_as_float(a.z & 0xffff0000u) * r * g1[1]);
;               o.w = cvt_pk_bf16(__uint_as_float(a.w << 16) * r * g1[2], __uint_as_float(a.w & 0xffff0000u) * r * g1[3]);
;               *(u32x4*)(MIX + tok * D + h * 128 + c16 + k * 8) = o;
;           } }
;         __syncthreads();
; #pragma unroll
;         for (int i = 0; i < 2; ++i) { const int ch = tid + i * 512, e = ch >> 3, part = ch & 7;
;             *(LAS u32x4*)(lds + C3_VT + e * R144 + part * 16) = *(const u32x4*)(VTH + ((size_t)b * 512 + h * 128 + e) * SEQ + j * 64 + part * 8); }
;         f32x4 o[4];
; #pragma unroll
;         for (int et = 0; et < 4; ++et) o[et] = (f32x4){0.f, 0.f, 0.f, 0.f};
;         float qv[16];
; #pragma unroll
;         for (int i = 0; i < 16; ++i) qv[i] = bf2f(QH[(tok0 + tq * 16 + i) * 512 + h * 128 + d]);
	global_load_dwordx4 v[224:227], v[22:23], off offset:16
	global_load_dwordx4 v[228:231], v[22:23], off
	global_load_dwordx4 v[232:235], v[30:31], off
	global_load_dwordx4 v[236:239], v[30:31], off offset:16
	v_lshl_add_u64 v[248:249], s[82:83], 0, v[52:53]
	v_lshlrev_b64 v[248:249], 10, v[248:249]
	v_lshl_add_u64 v[250:251], v[60:61], 0, s[90:91]
	v_lshl_add_u64 v[248:249], v[250:251], 0, v[248:249]
	v_mov_b32_e32 v252, 0x2000
	v_mov_b32_e32 v253, 0
	global_load_ushort v190, v[248:249], off
	global_load_ushort v191, v[248:249], off offset:1024
	global_load_ushort v192, v[248:249], off offset:2048
	global_load_ushort v193, v[248:249], off offset:3072
	v_lshl_add_u64 v[248:249], v[248:249], 0, v[252:253]
	global_load_ushort v194, v[248:249], off offset:-4096
	global_load_ushort v195, v[248:249], off offset:-3072
	global_load_ushort v196, v[248:249], off offset:-2048
	global_load_ushort v197, v[248:249], off offset:-1024
	global_load_ushort v198, v[248:249], off
	global_load_ushort v199, v[248:249], off offset:1024
	global_load_ushort v200, v[248:249], off offset:2048
	global_load_ushort v201, v[248:249], off offset:3072
	v_lshl_add_u64 v[248:249], v[248:249], 0, v[252:253]
	global_load_ushort v202, v[248:249], off offset:-4096
	global_load_ushort v203, v[248:249], off offset:-3072
	global_load_ushort v204, v[248:249], off offset:-2048
	global_load_ushort v205, v[248:249], off offset:-1024
	v_lshl_add_u64 v[250:251], s[92:93], 0, v[70:71]
	v_lshlrev_b64 v[250:251], 12, v[250:251]
	v_lshl_add_u64 v[250:251], v[84:85], 0, v[250:251]
	global_load_dwordx4 v[240:243], v[86:87], off
	global_load_dwordx4 v[244:247], v[250:251], off
.Lc3_havepf:
	s_waitcnt vmcnt(0)
	v_mov_b32_e32 v18, v224
	v_mov_b32_e32 v19, v225
	v_mov_b32_e32 v20, v226
	v_mov_b32_e32 v21, v227
	v_mov_b32_e32 v22, v228
	v_mov_b32_e32 v23, v229
	v_mov_b32_e32 v24, v230
	v_mov_b32_e32 v25, v231
	v_mov_b32_e32 v26, v232
	v_mov_b32_e32 v27, v233
	v_mov_b32_e32 v28, v234
	v_mov_b32_e32 v29, v235
	v_mov_b32_e32 v30, v236
	v_mov_b32_e32 v31, v237
	v_mov_b32_e32 v32, v238
	v_mov_b32_e32 v33, v239
	v_mov_b32_e32 v88, v23
	v_mov_b32_e32 v89, v24
	v_mov_b32_e32 v23, v25
	v_mov_b32_e32 v24, v20
	v_mov_b32_e32 v25, v18
	v_mov_b32_e32 v18, v21
	v_pk_add_f32 v[20:21], v[88:89], v[22:23]
	v_pk_add_f32 v[18:19], v[24:25], v[18:19]
	v_add_f32_e32 v89, v20, v21
	v_add_f32_e32 v19, v89, v19
	v_add_f32_e32 v18, v18, v19
	v_fmac_f32_e32 v90, 0x3b000000, v18
	v_mul_f32_e32 v18, 0x4b800000, v90
	v_cmp_gt_f32_e32 vcc, s85, v90
	v_lshlrev_b32_e32 v88, 16, v32
	v_and_b32_e32 v89, 0xffff0000, v32
	v_cndmask_b32_e32 v18, v90, v18, vcc
	v_rsq_f32_e32 v90, v18
	v_lshlrev_b32_e32 v20, 16, v26
	v_and_b32_e32 v21, 0xffff0000, v26
	v_lshlrev_b32_e32 v22, 16, v27
	v_mul_f32_e32 v32, 0x45800000, v90
	v_and_b32_e32 v23, 0xffff0000, v27
	v_lshlrev_b32_e32 v24, 16, v28
	v_and_b32_e32 v25, 0xffff0000, v28
	v_lshlrev_b32_e32 v26, 16, v29
	v_and_b32_e32 v27, 0xffff0000, v29
	v_cndmask_b32_e32 v32, v90, v32, vcc
	v_lshlrev_b32_e32 v28, 16, v30
	v_and_b32_e32 v29, 0xffff0000, v30
	v_lshlrev_b32_e32 v30, 16, v31
	v_and_b32_e32 v31, 0xffff0000, v31
	v_lshlrev_b32_e32 v18, 16, v33
	v_and_b32_e32 v19, 0xffff0000, v33
	v_pk_mul_f32 v[20:21], v[32:33], v[20:21] op_sel_hi:[0,1]
	v_pk_mul_f32 v[22:23], v[32:33], v[22:23] op_sel_hi:[0,1]
	v_pk_mul_f32 v[24:25], v[32:33], v[24:25] op_sel_hi:[0,1]
	v_pk_mul_f32 v[26:27], v[32:33], v[26:27] op_sel_hi:[0,1]
	v_pk_mul_f32 v[28:29], v[32:33], v[28:29] op_sel_hi:[0,1]
	v_pk_mul_f32 v[30:31], v[32:33], v[30:31] op_sel_hi:[0,1]
	v_pk_mul_f32 v[88:89], v[32:33], v[88:89] op_sel_hi:[0,1]
	v_pk_mul_f32 v[18:19], v[32:33], v[18:19] op_sel_hi:[0,1]
	v_pk_mul_f32 v[20:21], v[36:37], v[20:21]
	v_pk_mul_f32 v[22:23], v[38:39], v[22:23]
	v_pk_mul_f32 v[24:25], v[40:41], v[24:25]
	v_pk_mul_f32 v[26:27], v[42:43], v[26:27]
	v_pk_mul_f32 v[28:29], v[44:45], v[28:29]
	v_pk_mul_f32 v[30:31], v[46:47], v[30:31]
	v_pk_mul_f32 v[32:33], v[48:49], v[88:89]
	v_pk_mul_f32 v[36:37], v[50:51], v[18:19]
	v_cvt_pk_bf16_f32 v18, v20, v21
	v_cvt_pk_bf16_f32 v19, v22, v23
	v_cvt_pk_bf16_f32 v20, v24, v25
	v_cvt_pk_bf16_f32 v21, v26, v27
	v_cvt_pk_bf16_f32 v22, v28, v29
	v_cvt_pk_bf16_f32 v23, v30, v31
	v_cvt_pk_bf16_f32 v24, v32, v33
	v_cvt_pk_bf16_f32 v25, v36, v37
	global_store_dwordx4 v[82:83], v[18:21], off
	global_store_dwordx4 v[82:83], v[22:25], off offset:16
	v_lshl_add_u64 v[26:27], s[82:83], 0, v[52:53]
	v_lshl_add_u64 v[18:19], s[92:93], 0, v[70:71]
	v_lshlrev_b64 v[18:19], 12, v[18:19]
	v_or_b32_e32 v38, 2, v26
	v_mov_b32_e32 v39, v27
	v_or_b32_e32 v46, 4, v26
	v_mov_b32_e32 v47, v27
	v_lshl_add_u64 v[22:23], v[84:85], 0, v[18:19]
	v_lshl_add_u64 v[28:29], v[60:61], 0, s[90:91]
	v_lshlrev_b64 v[30:31], 10, v[26:27]
	v_or_b32_e32 v32, 1, v26
	v_mov_b32_e32 v33, v27
	v_lshlrev_b64 v[40:41], 10, v[38:39]
	v_or_b32_e32 v42, 3, v26
	v_mov_b32_e32 v43, v27
	v_lshlrev_b64 v[48:49], 10, v[46:47]
	v_or_b32_e32 v50, 5, v26
	v_mov_b32_e32 v51, v27
	v_or_b32_e32 v132, 6, v26
	v_mov_b32_e32 v133, v27
	v_or_b32_e32 v134, 7, v26
	v_mov_b32_e32 v135, v27
	s_barrier
; __device__ __forceinline__ void c3_phase(LAS unsigned char* lds, const bf16_t* __restrict__ QH, const bf16_t* __restrict__ LF, const bf16_t* __restrict__ VTH, const bf16_t* __restrict__ SIN, ...
;     ...
;         for (int i = 0; i < 2; ++i) { const int ch = tid + i * 512, e = ch >> 3, part = ch & 7;
;             *(LAS u32x4*)(lds + C3_VT + e * R144 + part * 16) = *(const u32x4*)(VTH + ((size_t)b * 512 + h * 128 + e) * SEQ + j * 64 + part * 8); }
;         f32x4 o[4];
; #pragma unroll
;         for (int et = 0; et < 4; ++et) o[et] = (f32x4){0.f, 0.f, 0.f, 0.f};
;         float qv[16];
; #pragma unroll
;         for (int i = 0; i < 16; ++i) qv[i] = bf2f(QH[(tok0 + tq * 16 + i) * 512 + h * 128 + d]);
; #pragma unroll 1
;         for (int dir = 0; dir < 2; ++dir) {
;             const size_t idx = ((size_t)(dir * NB + b) * 4 + h) * 32 + j;
;             float lfv[16], cs[16]; u32x4 stv[4];
; #pragma unroll
;             for (int i = 0; i < 16; ++i) lfv[i] = __uint_as_float(lfn[i] << 16);
; #pragma unroll
;             for (int i = 0; i < 4; ++i) stv[i] = stn[i];
;             float run = 0.f;
; #pragma unroll
;             for (int i = 0; i < 16; ++i) { run += lfv[i]; cs[i] = run; }
;             __syncthreads();
;             qtot[tq * 128 + d] = run;
; #pragma unroll
;             for (int i = 0; i < 4; ++i) { const int ch = tid + i * 512, e = ch >> 4, part = ch & 15;
;                 *(LAS u32x4*)(lds + C3_ST + e * R272 + part * 16) = stv[i]; }
;             __syncthreads();
;             const float q0 = qtot[d], q1 = qtot[128 + d], q2 = qtot[256 + d], q3 = qtot[384 + d];
;             const float pre = (tq > 0 ? q0 : 0.f) + (tq > 1 ? q1 : 0.f) + (tq > 2 ? q2 : 0.f), total = (q0 + q1) + (q2 + q3);
;             const float mref = dir == 0 ? (q0 + q1) : (q2 + q3);
; #pragma unroll
;             for (int i = 0; i < 16; ++i) {
;                 const int t = tq * 16 + i;
;                 const float bt = dir == 0 ? (pre + cs[i]) : (total - (pre + cs[i]) + lfv[i]);
;                 const float q = qv[i];
;                 const float key = 1.f - fexp(lfv[i]);
;                 *(LAS bf16_t*)(lds + C3_QT + t * R272 + d * 2) = f2bf(q * fexp(bt));
;                 *(LAS bf16_t*)(lds + C3_QH + t * R272 + d * 2) = f2bf(q * fexp(fminf(bt - mref, 80.f)));
;                 *(LAS bf16_t*)(lds + C3_KH + t * R272 + d * 2) = f2bf(key * fexp(fminf(mref - bt, 80.f)));
	v_lshl_add_u64 v[30:31], v[28:29], 0, v[30:31]
	v_lshlrev_b64 v[36:37], 10, v[32:33]
	v_lshl_add_u64 v[40:41], v[28:29], 0, v[40:41]
	v_lshlrev_b64 v[44:45], 10, v[42:43]
	v_lshl_add_u64 v[48:49], v[28:29], 0, v[48:49]
	v_lshlrev_b64 v[82:83], 10, v[50:51]
	v_lshlrev_b64 v[84:85], 10, v[132:133]
	v_lshlrev_b64 v[86:87], 10, v[134:135]
	v_lshl_add_u64 v[36:37], v[28:29], 0, v[36:37]
	v_lshl_add_u64 v[44:45], v[28:29], 0, v[44:45]
	v_lshl_add_u64 v[82:83], v[28:29], 0, v[82:83]
	v_lshl_add_u64 v[84:85], v[28:29], 0, v[84:85]
	v_lshl_add_u64 v[86:87], v[28:29], 0, v[86:87]
	v_or_b32_e32 v30, 8, v26
	v_mov_b32_e32 v31, v27
	v_or_b32_e32 v40, 9, v26
	v_mov_b32_e32 v41, v27
	v_or_b32_e32 v48, 10, v26
	v_mov_b32_e32 v49, v27
	v_or_b32_e32 v142, 11, v26
	v_mov_b32_e32 v143, v27
	v_or_b32_e32 v144, 12, v26
	v_mov_b32_e32 v145, v27
	v_or_b32_e32 v146, 13, v26
	v_mov_b32_e32 v147, v27
	v_or_b32_e32 v148, 14, v26
	v_mov_b32_e32 v149, v27
	v_or_b32_e32 v150, 15, v26
	v_mov_b32_e32 v151, v27
	v_lshlrev_b64 v[36:37], 10, v[30:31]
	v_lshlrev_b64 v[44:45], 10, v[40:41]
	v_lshlrev_b64 v[82:83], 10, v[48:49]
	v_lshlrev_b64 v[84:85], 10, v[142:143]
	v_lshlrev_b64 v[86:87], 10, v[144:145]
	v_lshlrev_b64 v[88:89], 10, v[146:147]
	v_lshlrev_b64 v[90:91], 10, v[148:149]
	v_lshlrev_b64 v[92:93], 10, v[150:151]
	v_lshl_add_u64 v[36:37], v[28:29], 0, v[36:37]
	v_lshl_add_u64 v[44:45], v[28:29], 0, v[44:45]
	v_lshl_add_u64 v[82:83], v[28:29], 0, v[82:83]
	v_lshl_add_u64 v[84:85], v[28:29], 0, v[84:85]
	v_lshl_add_u64 v[86:87], v[28:29], 0, v[86:87]
	v_lshl_add_u64 v[88:89], v[28:29], 0, v[88:89]
	v_lshl_add_u64 v[90:91], v[28:29], 0, v[90:91]
	v_lshl_add_u64 v[28:29], v[28:29], 0, v[92:93]
	v_readlane_b32 s80, v254, 20
	s_add_i32 s82, s89, s80
	s_cmpk_lt_i32 s82, 0x400
	s_cselect_b64 s[86:87], -1, 0
	s_cmpk_gt_i32 s82, 0x3ff
	s_cselect_b64 s[80:81], -1, 0
	s_lshl_b64 s[2:3], s[2:3], 7
	s_lshl_b32 s79, s79, 5
	s_or_b32 s2, s2, s79
	s_and_b32 s83, s82, 31
	s_or_b32 s2, s2, s78
	s_ashr_i32 s92, s82, 7
	s_bfe_u32 s89, s82, 0x20005
	s_lshl_b32 vcc_lo, s83, 6
	s_mov_b32 vcc_hi, s91
	s_lshl_b64 s[2:3], s[2:3], 15
	ds_write_b128 v179, v[240:243] offset:52224
	ds_write_b128 v180, v[244:247] offset:52224
	s_ashr_i32 s93, s92, 31
	v_lshl_add_u64 v[18:19], vcc, 0, v[52:53]
	s_lshl_b32 vcc_lo, s89, 8
	v_lshl_add_u64 v[20:21], v[62:63], 0, vcc
	v_lshlrev_b64 v[18:19], 11, v[18:19]
	v_lshl_add_u64 v[24:25], v[62:63], 0, s[90:91]
	v_lshlrev_b32_e32 v190, 16, v190
	v_lshlrev_b32_e32 v191, 16, v191
	v_lshlrev_b32_e32 v192, 16, v192
	v_lshlrev_b32_e32 v193, 16, v193
	v_lshlrev_b32_e32 v194, 16, v194
	v_lshlrev_b32_e32 v195, 16, v195
	v_writelane_b32 v254, s80, 30
	v_lshlrev_b32_e32 v196, 16, v196
	v_lshlrev_b32_e32 v197, 16, v197
	v_writelane_b32 v254, s81, 31
	s_lshl_b64 s[84:85], s[92:93], 7
	s_lshl_b32 s80, s89, 5
	s_or_b32 s80, s84, s80
	s_or_b32 s84, s80, s83
	s_lshl_b64 s[84:85], s[84:85], 15
	v_lshl_add_u64 v[22:23], v[66:67], 0, s[84:85]
	s_mov_b32 s81, s91
	v_lshl_add_u64 v[112:113], v[22:23], 0, v[72:73]
	v_lshl_add_u64 v[114:115], v[22:23], 0, v[74:75]
	v_lshl_add_u64 v[116:117], v[22:23], 0, v[76:77]
	v_lshl_add_u64 v[118:119], v[22:23], 0, v[78:79]
	v_lshlrev_b32_e32 v198, 16, v198
	v_lshlrev_b32_e32 v199, 16, v199
	v_lshlrev_b32_e32 v200, 16, v200
	v_lshlrev_b32_e32 v201, 16, v201
	v_lshlrev_b32_e32 v202, 16, v202
	v_lshlrev_b32_e32 v203, 16, v203
	v_lshlrev_b32_e32 v204, 16, v204
	v_lshlrev_b32_e32 v205, 16, v205
	v_lshl_add_u64 v[28:29], v[66:67], 0, s[2:3]
	s_mov_b64 s[2:3], 0x2000000
	v_lshl_add_u64 v[28:29], v[28:29], 0, s[2:3]
	s_lshl_b64 s[2:3], s[92:93], 22
	v_lshl_add_u64 v[20:21], v[20:21], 0, s[2:3]
	v_lshl_add_u64 v[82:83], v[20:21], 0, v[18:19]
	v_lshlrev_b64 v[18:19], 11, v[26:27]
	v_lshl_add_u64 v[120:121], v[24:25], 0, v[18:19]
	v_lshlrev_b64 v[18:19], 11, v[32:33]
	v_lshl_add_u64 v[122:123], v[24:25], 0, v[18:19]
	v_lshlrev_b64 v[18:19], 11, v[38:39]
	s_mov_b64 s[2:3], 0x1000
	v_lshl_add_u64 v[124:125], v[24:25], 0, v[18:19]
	v_lshlrev_b64 v[18:19], 11, v[42:43]
	v_lshl_add_u64 v[84:85], v[82:83], 0, s[2:3]
	s_mov_b64 s[2:3], 0x1800
	v_lshl_add_u64 v[126:127], v[24:25], 0, v[18:19]
	v_lshlrev_b64 v[18:19], 11, v[46:47]
	v_lshl_add_u64 v[86:87], v[82:83], 0, s[2:3]
	s_mov_b64 s[2:3], 0x2000
	v_lshl_add_u64 v[128:129], v[24:25], 0, v[18:19]
	v_lshlrev_b64 v[18:19], 11, v[50:51]
	v_lshl_add_u64 v[88:89], v[82:83], 0, s[2:3]
	s_mov_b64 s[2:3], 0x2800
	v_lshl_add_u64 v[130:131], v[24:25], 0, v[18:19]
	v_lshlrev_b64 v[18:19], 11, v[132:133]
	v_lshl_add_u64 v[90:91], v[82:83], 0, s[2:3]
	s_mov_b64 s[2:3], 0x3000
	v_lshl_add_u64 v[132:133], v[24:25], 0, v[18:19]
	v_lshlrev_b64 v[18:19], 11, v[134:135]
	v_lshl_add_u64 v[92:93], v[82:83], 0, s[2:3]
	s_mov_b64 s[2:3], 0x3800
	v_lshl_add_u64 v[134:135], v[24:25], 0, v[18:19]
	v_lshlrev_b64 v[18:19], 11, v[30:31]
	v_lshl_add_u64 v[94:95], v[82:83], 0, s[2:3]
	s_mov_b64 s[2:3], 0x4000
	v_lshl_add_u64 v[136:137], v[24:25], 0, v[18:19]
	v_lshlrev_b64 v[18:19], 11, v[40:41]
	v_lshl_add_u64 v[96:97], v[82:83], 0, s[2:3]
	s_mov_b64 s[2:3], 0x4800
	v_lshl_add_u64 v[138:139], v[24:25], 0, v[18:19]
	v_lshlrev_b64 v[18:19], 11, v[48:49]
	v_lshl_add_u64 v[98:99], v[82:83], 0, s[2:3]
	s_mov_b64 s[2:3], 0x5000
	v_lshl_add_u64 v[140:141], v[24:25], 0, v[18:19]
	v_lshlrev_b64 v[18:19], 11, v[142:143]
	v_lshl_add_u64 v[100:101], v[82:83], 0, s[2:3]
	s_mov_b64 s[2:3], 0x5800
	v_lshl_add_u64 v[142:143], v[24:25], 0, v[18:19]
	v_lshlrev_b64 v[18:19], 11, v[144:145]
	v_lshl_add_u64 v[102:103], v[82:83], 0, s[2:3]
	s_mov_b64 s[2:3], 0x6000
	v_lshl_add_u64 v[144:145], v[24:25], 0, v[18:19]
	v_lshlrev_b64 v[18:19], 11, v[146:147]
	v_lshl_add_u64 v[104:105], v[82:83], 0, s[2:3]
	s_mov_b64 s[2:3], 0x6800
	v_lshl_add_u64 v[146:147], v[24:25], 0, v[18:19]
	v_lshlrev_b64 v[18:19], 11, v[148:149]
	v_lshl_add_u64 v[106:107], v[82:83], 0, s[2:3]
	s_mov_b64 s[2:3], 0x7000
	v_lshl_add_u64 v[148:149], v[24:25], 0, v[18:19]
	v_lshlrev_b64 v[18:19], 11, v[150:151]
	v_lshl_add_u64 v[108:109], v[82:83], 0, s[2:3]
	s_mov_b64 s[2:3], 0x7800
	v_lshl_add_u64 v[150:151], v[24:25], 0, v[18:19]
	v_mov_b32_e32 v18, 0
	v_lshl_add_u64 v[110:111], v[82:83], 0, s[2:3]
	v_lshl_add_u64 v[152:153], v[28:29], 0, v[72:73]
	v_lshl_add_u64 v[154:155], v[28:29], 0, v[74:75]
	v_lshl_add_u64 v[156:157], v[28:29], 0, v[76:77]
	v_lshl_add_u64 v[158:159], v[28:29], 0, v[78:79]
	s_mov_b64 s[2:3], -1
	v_mov_b32_e32 v19, v18
	v_mov_b32_e32 v20, v18
	v_mov_b32_e32 v21, v18
	v_mov_b32_e32 v26, v18
	v_mov_b32_e32 v27, v18
	v_mov_b32_e32 v28, v18
	v_mov_b32_e32 v29, v18
	v_mov_b32_e32 v22, v18
	v_mov_b32_e32 v23, v18
	v_mov_b32_e32 v24, v18
	v_mov_b32_e32 v25, v18
	v_mov_b32_e32 v30, v18
	v_mov_b32_e32 v31, v18
	v_mov_b32_e32 v32, v18
	v_mov_b32_e32 v33, v18
	s_branch .LBB0_1097

; #define LAS __attribute__((address_space(3)))
; __device__ __forceinline__ bf16_t f2bf(float f) { unsigned u = __float_as_uint(f); u += 0x7FFFu + ((u >> 16) & 1u); return (bf16_t)(u >> 16); }
; __device__ __forceinline__ float fexp(float x) { return __builtin_amdgcn_exp2f(x * 1.4426950408889634f); }
; #define lds lds_hidden(lds0)
; __device__ __forceinline__ void c3_phase(LAS unsigned char* lds, const bf16_t* __restrict__ QH, const bf16_t* __restrict__ LF, const bf16_t* __restrict__ VTH, const bf16_t* __restrict__ SIN, ...
;     ...
;             for (int i = 0; i < 16; ++i) lfv[i] = __uint_as_float(lfn[i] << 16);
; #pragma unroll
;             for (int i = 0; i < 4; ++i) stv[i] = stn[i];
;             float run = 0.f;
; #pragma unroll
;             for (int i = 0; i < 16; ++i) { run += lfv[i]; cs[i] = run; }
;             __syncthreads();
;             qtot[tq * 128 + d] = run;
; #pragma unroll
;             for (int i = 0; i < 4; ++i) { const int ch = tid + i * 512, e = ch >> 4, part = ch & 15;
;                 *(LAS u32x4*)(lds + C3_ST + e * R272 + part * 16) = stv[i]; }
;             __syncthreads();
;             const float q0 = qtot[d], q1 = qtot[128 + d], q2 = qtot[256 + d], q3 = qtot[384 + d];
;             const float pre = (tq > 0 ? q0 : 0.f) + (tq > 1 ? q1 : 0.f) + (tq > 2 ? q2 : 0.f), total = (q0 + q1) + (q2 + q3);
;             const float mref = dir == 0 ? (q0 + q1) : (q2 + q3);
; #pragma unroll
;             for (int i = 0; i < 16; ++i) {
;                 const int t = tq * 16 + i;
;                 const float bt = dir == 0 ? (pre + cs[i]) : (total - (pre + cs[i]) + lfv[i]);
;                 const float q = qv[i];
;                 const float key = 1.f - fexp(lfv[i]);
;                 *(LAS bf16_t*)(lds + C3_QT + t * R272 + d * 2) = f2bf(q * fexp(bt));
;                 *(LAS bf16_t*)(lds + C3_QH + t * R272 + d * 2) = f2bf(q * fexp(fminf(bt - mref, 80.f)));
;                 *(LAS bf16_t*)(lds + C3_KH + t * R272 + d * 2) = f2bf(key * fexp(fminf(mref - bt, 80.f)));
.LBB0_1097:
	s_waitcnt vmcnt(19)
	v_lshlrev_b32_e32 v215, 16, v162
	v_mul_f32_e32 v215, 0x3fb8aa3b, v215
	s_waitcnt vmcnt(18)
	v_lshlrev_b32_e32 v220, 16, v164
	v_mul_f32_e32 v220, 0x3fb8aa3b, v220
	v_add_f32_e32 v224, 0, v215
	s_waitcnt vmcnt(17)
	v_lshlrev_b32_e32 v221, 16, v65
	v_mul_f32_e32 v221, 0x3fb8aa3b, v221
	v_add_f32_e32 v225, v224, v220
	s_waitcnt vmcnt(16)
	v_lshlrev_b32_e32 v222, 16, v166
	v_mul_f32_e32 v222, 0x3fb8aa3b, v222
	v_add_f32_e32 v226, v225, v221
	s_waitcnt vmcnt(15)
	v_lshlrev_b32_e32 v223, 16, v160
	v_mul_f32_e32 v223, 0x3fb8aa3b, v223
	v_add_f32_e32 v227, v226, v222
	s_waitcnt vmcnt(14)
	v_lshlrev_b32_e32 v213, 16, v161
	v_mul_f32_e32 v213, 0x3fb8aa3b, v213
	v_add_f32_e32 v228, v227, v223
	s_waitcnt vmcnt(13)
	v_lshlrev_b32_e32 v211, 16, v163
	v_mul_f32_e32 v211, 0x3fb8aa3b, v211
	v_add_f32_e32 v214, v228, v213
	s_waitcnt vmcnt(12)
	v_lshlrev_b32_e32 v209, 16, v169
	v_mul_f32_e32 v209, 0x3fb8aa3b, v209
	v_add_f32_e32 v212, v214, v211
	s_waitcnt vmcnt(11)
	v_lshlrev_b32_e32 v207, 16, v165
	v_mul_f32_e32 v207, 0x3fb8aa3b, v207
	v_add_f32_e32 v210, v212, v209
	s_waitcnt vmcnt(10)
	v_lshlrev_b32_e32 v51, 16, v167
	v_mul_f32_e32 v51, 0x3fb8aa3b, v51
	v_add_f32_e32 v208, v210, v207
	s_waitcnt vmcnt(9)
	v_lshlrev_b32_e32 v49, 16, v168
	v_mul_f32_e32 v49, 0x3fb8aa3b, v49
	v_add_f32_e32 v206, v208, v51
	s_waitcnt vmcnt(8)
	v_lshlrev_b32_e32 v47, 16, v172
	v_mul_f32_e32 v47, 0x3fb8aa3b, v47
	v_add_f32_e32 v50, v206, v49
	s_waitcnt vmcnt(7)
	v_lshlrev_b32_e32 v45, 16, v170
	v_mul_f32_e32 v45, 0x3fb8aa3b, v45
	v_add_f32_e32 v48, v50, v47
	s_waitcnt vmcnt(6)
	v_lshlrev_b32_e32 v43, 16, v171
	v_mul_f32_e32 v43, 0x3fb8aa3b, v43
	v_add_f32_e32 v46, v48, v45
	s_waitcnt vmcnt(5)
	v_lshlrev_b32_e32 v41, 16, v173
	v_mul_f32_e32 v41, 0x3fb8aa3b, v41
	v_add_f32_e32 v44, v46, v43
	s_waitcnt vmcnt(4)
	v_lshlrev_b32_e32 v37, 16, v174
	v_mul_f32_e32 v37, 0x3fb8aa3b, v37
	v_add_f32_e32 v42, v44, v41
	v_add_f32_e32 v38, v42, v37
	s_waitcnt lgkmcnt(0)
	s_barrier
	ds_write_b32 v175, v38
	s_waitcnt vmcnt(3)
	ds_write_b128 v181, v[2:5]
	s_waitcnt vmcnt(2)
	ds_write_b128 v182, v[6:9]
	s_waitcnt vmcnt(1)
	ds_write_b128 v183, v[10:13]
	s_waitcnt vmcnt(0)
	ds_write_b128 v184, v[14:17]
	s_waitcnt lgkmcnt(0)
	s_barrier
	ds_read2st64_b32 v[216:217], v176 offset1:2
	ds_read2st64_b32 v[218:219], v176 offset0:4 offset1:6
	s_xor_b64 s[78:79], s[2:3], -1
	s_and_b64 vcc, exec, s[78:79]
	s_mov_b64 s[92:93], -1
	s_waitcnt lgkmcnt(1)
	v_cndmask_b32_e64 v36, 0, v216, s[4:5]
	v_cndmask_b32_e64 v39, 0, v217, s[6:7]
	v_add_f32_e32 v36, v36, v39
	s_waitcnt lgkmcnt(0)
	v_cndmask_b32_e64 v39, 0, v218, s[8:9]
	v_add_f32_e32 v39, v36, v39
	v_add_f32_e32 v36, v216, v217
	v_add_f32_e32 v216, v218, v219
	v_add_f32_e32 v40, v36, v216
	v_cndmask_b32_e64 v231, -1.0, 1.0, s[2:3]
	v_cndmask_b32_e64 v232, v40, 0, s[2:3]
	v_cndmask_b32_e64 v233, 1.0, 0, s[2:3]
	v_cndmask_b32_e64 v36, v216, v36, s[2:3]
	v_add_f32_e32 v216, v224, v39
	v_fma_f32 v217, v231, v216, v232
	v_fma_f32 v216, v233, v215, v217
	v_exp_f32_e32 v217, v216
	v_exp_f32_e32 v215, v215
	v_add_f32_e32 v214, v214, v39
	v_mul_f32_e32 v234, v217, v190
	v_sub_f32_e32 v217, v216, v36
	v_max_f32_e32 v216, 0xc2e6d4ca, v217
	v_exp_f32_e64 v216, -v216
	v_min_f32_e32 v217, 0x42e6d4ca, v217
	v_exp_f32_e32 v217, v217
	v_fma_f32 v215, -v215, v216, v216
	v_cvt_pk_bf16_f32 v215, v215, v215
	ds_write_b16 v185, v215 offset:34816
	v_add_f32_e32 v215, v225, v39
	v_mul_f32_e32 v217, v217, v190
	v_fma_f32 v216, v231, v215, v232
	v_cvt_pk_bf16_f32 v217, v234, v217
	v_fma_f32 v215, v233, v220, v216
	ds_write_b16 v185, v217
	ds_write_b16_d16_hi v185, v217 offset:17408
	v_exp_f32_e32 v217, v215
	v_exp_f32_e32 v216, v220
	v_add_f32_e32 v212, v212, v39
	v_mul_f32_e32 v235, v217, v191
	v_sub_f32_e32 v217, v215, v36
	v_max_f32_e32 v215, 0xc2e6d4ca, v217
	v_exp_f32_e64 v215, -v215
	v_min_f32_e32 v217, 0x42e6d4ca, v217
	v_exp_f32_e32 v217, v217
	v_fma_f32 v215, -v216, v215, v215
	v_cvt_pk_bf16_f32 v215, v215, v215
	ds_write_b16 v185, v215 offset:35088
	v_add_f32_e32 v215, v226, v39
	v_mul_f32_e32 v217, v217, v191
	v_fma_f32 v216, v231, v215, v232
	v_cvt_pk_bf16_f32 v217, v235, v217
	v_fma_f32 v215, v233, v221, v216
	ds_write_b16 v185, v217 offset:272
	ds_write_b16_d16_hi v185, v217 offset:17680
	v_exp_f32_e32 v217, v215
	v_exp_f32_e32 v216, v221
	v_add_f32_e32 v210, v210, v39
	v_mul_f32_e32 v236, v217, v192
	v_sub_f32_e32 v217, v215, v36
	v_max_f32_e32 v215, 0xc2e6d4ca, v217
	v_exp_f32_e64 v215, -v215
	v_min_f32_e32 v217, 0x42e6d4ca, v217
	v_exp_f32_e32 v217, v217
	v_fma_f32 v215, -v216, v215, v215
	v_cvt_pk_bf16_f32 v215, v215, v215
	ds_write_b16 v185, v215 offset:35360
	v_add_f32_e32 v215, v227, v39
	v_mul_f32_e32 v217, v217, v192
	v_fma_f32 v216, v231, v215, v232
	v_cvt_pk_bf16_f32 v217, v236, v217
	v_fma_f32 v215, v233, v222, v216
	ds_write_b16 v185, v217 offset:544
	ds_write_b16_d16_hi v185, v217 offset:17952
	v_exp_f32_e32 v217, v215
	v_exp_f32_e32 v216, v222
	v_add_f32_e32 v208, v208, v39
	v_mul_f32_e32 v237, v217, v193
	v_sub_f32_e32 v217, v215, v36
	v_max_f32_e32 v215, 0xc2e6d4ca, v217
	v_exp_f32_e64 v215, -v215
	v_min_f32_e32 v217, 0x42e6d4ca, v217
	v_exp_f32_e32 v217, v217
	v_fma_f32 v215, -v216, v215, v215
	v_cvt_pk_bf16_f32 v215, v215, v215
	ds_write_b16 v185, v215 offset:35632
	v_add_f32_e32 v215, v228, v39
	v_mul_f32_e32 v217, v217, v193
	v_fma_f32 v216, v231, v215, v232
	v_cvt_pk_bf16_f32 v217, v237, v217
	v_fma_f32 v215, v233, v223, v216
	ds_write_b16 v185, v217 offset:816
	ds_write_b16_d16_hi v185, v217 offset:18224
	v_exp_f32_e32 v217, v215
	v_exp_f32_e32 v216, v223
	v_add_f32_e32 v206, v206, v39
	v_mul_f32_e32 v238, v217, v194
; #define LAS __attribute__((address_space(3)))
; __device__ __forceinline__ bf16_t f2bf(float f) { unsigned u = __float_as_uint(f); u += 0x7FFFu + ((u >> 16) & 1u); return (bf16_t)(u >> 16); }
; __device__ __forceinline__ float fexp(float x) { return __builtin_amdgcn_exp2f(x * 1.4426950408889634f); }
; #define lds lds_hidden(lds0)
; __device__ __forceinline__ void c3_phase(LAS unsigned char* lds, const bf16_t* __restrict__ QH, const bf16_t* __restrict__ LF, const bf16_t* __restrict__ VTH, const bf16_t* __restrict__ SIN, ...
;     ...
;             for (int i = 0; i < 16; ++i) {
;                 const int t = tq * 16 + i;
;                 const float bt = dir == 0 ? (pre + cs[i]) : (total - (pre + cs[i]) + lfv[i]);
;                 const float q = qv[i];
;                 const float key = 1.f - fexp(lfv[i]);
;                 *(LAS bf16_t*)(lds + C3_QT + t * R272 + d * 2) = f2bf(q * fexp(bt));
;                 *(LAS bf16_t*)(lds + C3_QH + t * R272 + d * 2) = f2bf(q * fexp(fminf(bt - mref, 80.f)));
;                 *(LAS bf16_t*)(lds + C3_KH + t * R272 + d * 2) = f2bf(key * fexp(fminf(mref - bt, 80.f)));
;             }
;             __syncthreads();
	v_sub_f32_e32 v217, v215, v36
	v_max_f32_e32 v215, 0xc2e6d4ca, v217
	v_exp_f32_e64 v215, -v215
	v_add_f32_e32 v50, v50, v39
	v_add_f32_e32 v48, v48, v39
	v_fma_f32 v215, -v216, v215, v215
	v_cvt_pk_bf16_f32 v215, v215, v215
	ds_write_b16 v185, v215 offset:35904
	v_fma_f32 v215, v231, v214, v232
	v_fma_f32 v214, v233, v213, v215
	v_exp_f32_e32 v215, v214
	v_exp_f32_e32 v213, v213
	v_add_f32_e32 v46, v46, v39
	v_mul_f32_e32 v239, v215, v195
	v_sub_f32_e32 v215, v214, v36
	v_max_f32_e32 v214, 0xc2e6d4ca, v215
	v_exp_f32_e64 v214, -v214
	v_add_f32_e32 v44, v44, v39
	v_add_f32_e32 v42, v42, v39
	v_fma_f32 v213, -v213, v214, v214
	v_cvt_pk_bf16_f32 v213, v213, v213
	ds_write_b16 v185, v213 offset:36176
	v_fma_f32 v213, v231, v212, v232
	v_fma_f32 v212, v233, v211, v213
	v_exp_f32_e32 v213, v212
	v_exp_f32_e32 v211, v211
	v_add_f32_e32 v38, v38, v39
	v_mul_f32_e32 v240, v213, v196
	v_sub_f32_e32 v213, v212, v36
	v_max_f32_e32 v212, 0xc2e6d4ca, v213
	v_exp_f32_e64 v212, -v212
	v_fma_f32 v39, v231, v38, v232
	v_fma_f32 v211, -v211, v212, v212
	v_cvt_pk_bf16_f32 v211, v211, v211
	ds_write_b16 v185, v211 offset:36448
	v_fma_f32 v211, v231, v210, v232
	v_fma_f32 v210, v233, v209, v211
	v_exp_f32_e32 v211, v210
	v_exp_f32_e32 v209, v209
	v_fma_f32 v38, v233, v37, v39
	v_mul_f32_e32 v241, v211, v197
	v_sub_f32_e32 v211, v210, v36
	v_max_f32_e32 v210, 0xc2e6d4ca, v211
	v_exp_f32_e64 v210, -v210
	v_exp_f32_e32 v39, v38
	v_fma_f32 v209, -v209, v210, v210
	v_cvt_pk_bf16_f32 v209, v209, v209
	ds_write_b16 v185, v209 offset:36720
	v_fma_f32 v209, v231, v208, v232
	v_fma_f32 v208, v233, v207, v209
	v_exp_f32_e32 v209, v208
	v_exp_f32_e32 v207, v207
	v_mul_f32_e32 v39, v39, v205
	v_mul_f32_e32 v242, v209, v198
	v_sub_f32_e32 v209, v208, v36
	v_max_f32_e32 v208, 0xc2e6d4ca, v209
	v_exp_f32_e64 v208, -v208
	v_min_f32_e32 v217, 0x42e6d4ca, v217
	v_min_f32_e32 v215, 0x42e6d4ca, v215
	v_fma_f32 v207, -v207, v208, v208
	v_cvt_pk_bf16_f32 v207, v207, v207
	ds_write_b16 v185, v207 offset:36992
	v_fma_f32 v207, v231, v206, v232
	v_fma_f32 v206, v233, v51, v207
	v_exp_f32_e32 v207, v206
	v_exp_f32_e32 v51, v51
	v_min_f32_e32 v213, 0x42e6d4ca, v213
	v_mul_f32_e32 v243, v207, v199
	v_sub_f32_e32 v207, v206, v36
	v_max_f32_e32 v206, 0xc2e6d4ca, v207
	v_exp_f32_e64 v206, -v206
	v_min_f32_e32 v211, 0x42e6d4ca, v211
	v_min_f32_e32 v209, 0x42e6d4ca, v209
	v_fma_f32 v51, -v51, v206, v206
	v_cvt_pk_bf16_f32 v51, v51, v51
	ds_write_b16 v185, v51 offset:37264
	v_fma_f32 v51, v231, v50, v232
	v_fma_f32 v50, v233, v49, v51
	v_exp_f32_e32 v51, v50
	v_exp_f32_e32 v49, v49
	v_min_f32_e32 v207, 0x42e6d4ca, v207
	v_mul_f32_e32 v244, v51, v200
	v_sub_f32_e32 v51, v50, v36
	v_max_f32_e32 v50, 0xc2e6d4ca, v51
	v_exp_f32_e64 v50, -v50
	v_min_f32_e32 v51, 0x42e6d4ca, v51
	v_fma_f32 v49, -v49, v50, v50
	v_cvt_pk_bf16_f32 v49, v49, v49
	ds_write_b16 v185, v49 offset:37536
	v_fma_f32 v49, v231, v48, v232
	v_fma_f32 v48, v233, v47, v49
	v_exp_f32_e32 v49, v48
	v_exp_f32_e32 v47, v47
	v_mul_f32_e32 v245, v49, v201
	v_sub_f32_e32 v49, v48, v36
	v_max_f32_e32 v48, 0xc2e6d4ca, v49
	v_exp_f32_e64 v48, -v48
	v_min_f32_e32 v49, 0x42e6d4ca, v49
	v_fma_f32 v47, -v47, v48, v48
	v_cvt_pk_bf16_f32 v47, v47, v47
	ds_write_b16 v185, v47 offset:37808
	v_fma_f32 v47, v231, v46, v232
	v_fma_f32 v46, v233, v45, v47
	v_exp_f32_e32 v47, v46
	v_exp_f32_e32 v45, v45
	v_mul_f32_e32 v246, v47, v202
	v_sub_f32_e32 v47, v46, v36
	v_max_f32_e32 v46, 0xc2e6d4ca, v47
	v_exp_f32_e64 v46, -v46
	v_min_f32_e32 v47, 0x42e6d4ca, v47
	v_fma_f32 v45, -v45, v46, v46
	v_cvt_pk_bf16_f32 v45, v45, v45
	ds_write_b16 v185, v45 offset:38080
	v_fma_f32 v45, v231, v44, v232
	v_fma_f32 v44, v233, v43, v45
	v_exp_f32_e32 v45, v44
	v_exp_f32_e32 v43, v43
	v_mul_f32_e32 v247, v45, v203
	v_sub_f32_e32 v45, v44, v36
	v_max_f32_e32 v44, 0xc2e6d4ca, v45
	v_exp_f32_e64 v44, -v44
	v_min_f32_e32 v45, 0x42e6d4ca, v45
	v_fma_f32 v43, -v43, v44, v44
	v_cvt_pk_bf16_f32 v43, v43, v43
	ds_write_b16 v185, v43 offset:38352
	v_fma_f32 v43, v231, v42, v232
	v_fma_f32 v42, v233, v41, v43
	v_exp_f32_e32 v43, v42
	v_cvt_pk_bf16_f32 v39, v39, v39
	ds_write_b16 v185, v39 offset:4080
	v_mul_f32_e32 v248, v43, v204
	v_sub_f32_e32 v43, v42, v36
	v_max_f32_e32 v42, 0xc2e6d4ca, v43
	v_sub_f32_e32 v39, v38, v36
	v_max_f32_e32 v36, 0xc2e6d4ca, v39
	v_min_f32_e32 v43, 0x42e6d4ca, v43
	v_min_f32_e32 v39, 0x42e6d4ca, v39
	v_exp_f32_e32 v41, v41
	v_exp_f32_e32 v37, v37
	v_exp_f32_e32 v217, v217
	v_exp_f32_e32 v215, v215
	v_exp_f32_e32 v213, v213
	v_exp_f32_e32 v211, v211
	v_exp_f32_e32 v209, v209
	v_exp_f32_e32 v207, v207
	v_exp_f32_e32 v51, v51
	v_exp_f32_e32 v49, v49
	v_exp_f32_e32 v47, v47
	v_exp_f32_e32 v45, v45
	v_exp_f32_e32 v43, v43
	v_exp_f32_e64 v42, -v42
	v_exp_f32_e32 v39, v39
	v_exp_f32_e64 v36, -v36
	v_mul_f32_e32 v217, v217, v194
	v_mul_f32_e32 v215, v215, v195
	v_mul_f32_e32 v213, v213, v196
	v_mul_f32_e32 v211, v211, v197
	v_mul_f32_e32 v209, v209, v198
	v_mul_f32_e32 v207, v207, v199
	v_mul_f32_e32 v51, v51, v200
	v_mul_f32_e32 v49, v49, v201
	v_mul_f32_e32 v47, v47, v202
	v_mul_f32_e32 v45, v45, v203
	v_mul_f32_e32 v43, v43, v204
	v_fma_f32 v41, -v41, v42, v42
	v_mul_f32_e32 v39, v39, v205
	v_fma_f32 v36, -v37, v36, v36
	v_cvt_pk_bf16_f32 v217, v238, v217
	v_cvt_pk_bf16_f32 v215, v239, v215
	v_cvt_pk_bf16_f32 v213, v240, v213
	v_cvt_pk_bf16_f32 v211, v241, v211
	v_cvt_pk_bf16_f32 v209, v242, v209
	v_cvt_pk_bf16_f32 v207, v243, v207
	v_cvt_pk_bf16_f32 v51, v244, v51
	v_cvt_pk_bf16_f32 v49, v245, v49
	v_cvt_pk_bf16_f32 v47, v246, v47
	v_cvt_pk_bf16_f32 v45, v247, v45
	v_cvt_pk_bf16_f32 v43, v248, v43
	v_cvt_pk_bf16_f32 v41, v41, v41
	v_cvt_pk_bf16_f32 v39, v39, v39
	v_cvt_pk_bf16_f32 v36, v36, v36
	ds_write_b16 v185, v217 offset:1088
	ds_write_b16_d16_hi v185, v217 offset:18496
	ds_write_b16 v185, v215 offset:1360
	ds_write_b16_d16_hi v185, v215 offset:18768
	ds_write_b16 v185, v213 offset:1632
	ds_write_b16_d16_hi v185, v213 offset:19040
	ds_write_b16 v185, v211 offset:1904
	ds_write_b16_d16_hi v185, v211 offset:19312
	ds_write_b16 v185, v209 offset:2176
	ds_write_b16_d16_hi v185, v209 offset:19584
	ds_write_b16 v185, v207 offset:2448
	ds_write_b16_d16_hi v185, v207 offset:19856
	ds_write_b16 v185, v51 offset:2720
	ds_write_b16_d16_hi v185, v51 offset:20128
	ds_write_b16 v185, v49 offset:2992
	ds_write_b16_d16_hi v185, v49 offset:20400
	ds_write_b16 v185, v47 offset:3264
	ds_write_b16_d16_hi v185, v47 offset:20672
	ds_write_b16 v185, v45 offset:3536
	ds_write_b16_d16_hi v185, v45 offset:20944
	ds_write_b16 v185, v43 offset:3808
	ds_write_b16_d16_hi v185, v43 offset:21216
	ds_write_b16 v185, v41 offset:38624
	ds_write_b16 v185, v39 offset:21488
	ds_write_b16 v185, v36 offset:38896
	s_waitcnt lgkmcnt(0)
	s_barrier
; #define LAS __attribute__((address_space(3)))
; __device__ __forceinline__ float bf2f(bf16_t b) { return __uint_as_float(((unsigned)b) << 16); }
; #define lds lds_hidden(lds0)
; __device__ __forceinline__ void c3_phase(LAS unsigned char* lds, const bf16_t* __restrict__ QH, const bf16_t* __restrict__ LF, const bf16_t* __restrict__ VTH, const bf16_t* __restrict__ SIN, ...
;     ...
;     if (c < NB * 4 * 32) C3_PREFETCH(c, 0);
;     for (int item = c; item < NB * 4 * 32; item += G) {
;         const int b = item >> 7, h = (item >> 5) & 3, j = item & 31;
;         const size_t tok0 = (size_t)b * SEQ + j * 64;
;         { const int t = tid >> 3, c16 = (tid & 7) * 16; const size_t tok = tok0 + t;
;           const f32x4 s0 = *(const f32x4*)(SSQ + tok * 8), s1 = *(const f32x4*)(SSQ + tok * 8 + 4);
;           const float r = rsqrtf(((s0[0] + s0[1]) + (s0[2] + s0[3]) + (s1[0] + s1[1]) + (s1[2] + s1[3])) * (1.f / 512) + kf(EPS));
; #pragma unroll
;           for (int k = 0; k < 2; ++k) {
;               const u32x4 a = *(const u32x4*)(AO + tok * 512 + h * 128 + c16 + k * 8);
;               const f32x4 g0 = *(const f32x4*)(attn_gain + h * 128 + c16 + k * 8), g1 = *(const f32x4*)(attn_gain + h * 128 + c16 + k * 8 + 4);
;               u32x4 o;
;               o.x = cvt_pk_bf16(__uint_as_float(a.x << 16) * r * g0[0], __uint_as_float(a.x & 0xffff0000u) * r * g0[1]);
;               o.y = cvt_pk_bf16(__uint_as_float(a.y << 16) * r * g0[2], __uint_as_float(a.y & 0xffff0000u) * r * g0[3]);
;               o.z = cvt_pk_bf16(__uint_as_float(a.z << 16) * r * g1[0], __uint_as_float(a.z & 0xffff0000u) * r * g1[1]);
;               o.w = cvt_pk_bf16(__uint_as_float(a.w << 16) * r * g1[2], __uint_as_float(a.w & 0xffff0000u) * r * g1[3]);
;               *(u32x4*)(MIX + tok * D + h * 128 + c16 + k * 8) = o;
;           } }
;         __syncthreads();
; #pragma unroll
;         for (int i = 0; i < 2; ++i) { const int ch = tid + i * 512, e = ch >> 3, part = ch & 7;
;             *(LAS u32x4*)(lds + C3_VT + e * R144 + part * 16) = *(const u32x4*)(VTH + ((size_t)b * 512 + h * 128 + e) * SEQ + j * 64 + part * 8); }
;         f32x4 o[4];
; #pragma unroll
;         for (int et = 0; et < 4; ++et) o[et] = (f32x4){0.f, 0.f, 0.f, 0.f};
;         float qv[16];
; #pragma unroll
;         for (int i = 0; i < 16; ++i) qv[i] = bf2f(QH[(tok0 + tq * 16 + i) * 512 + h * 128 + d]);
	s_cbranch_vccz .LBB0_1101
	s_andn2_b64 vcc, exec, s[86:87]
	s_cbranch_vccnz .LBB0_1100
	global_load_ushort v162, v[82:83], off
	global_load_ushort v164, v[82:83], off offset:2048
	global_load_ushort v65, v[84:85], off
	global_load_ushort v166, v[86:87], off
	global_load_ushort v160, v[88:89], off
	global_load_ushort v161, v[90:91], off
	global_load_ushort v163, v[92:93], off
	global_load_ushort v169, v[94:95], off
	global_load_ushort v165, v[96:97], off
	global_load_ushort v167, v[98:99], off
	global_load_ushort v168, v[100:101], off
	global_load_ushort v172, v[102:103], off
	global_load_ushort v170, v[104:105], off
	global_load_ushort v171, v[106:107], off
	global_load_ushort v173, v[108:109], off
	global_load_ushort v174, v[110:111], off
	global_load_dwordx4 v[2:5], v[112:113], off nt
	global_load_dwordx4 v[6:9], v[114:115], off nt
	global_load_dwordx4 v[10:13], v[116:117], off nt
	global_load_dwordx4 v[14:17], v[118:119], off nt
	v_mov_b32_e32 v95, s82
	v_readlane_b32 vcc_lo, v254, 18
	v_readlane_b32 vcc_hi, v254, 19
	v_ashrrev_i32_e32 v248, 7, v95
	v_and_b32_e32 v249, 31, v95
	v_bfe_u32 v250, v95, 5, 2
	v_lshlrev_b32_e32 v251, 11, v248
	v_lshl_or_b32 v251, v249, 6, v251
	v_add_u32_e32 v252, v251, v54
	v_mov_b32_e32 v253, 0
	v_lshlrev_b64 v[244:245], 5, v[252:253]
	v_lshl_add_u64 v[244:245], vcc, 0, v[244:245]
	v_readlane_b32 vcc_lo, v254, 16
	v_readlane_b32 vcc_hi, v254, 17
	global_load_dwordx4 v[224:227], v[244:245], off offset:16
	global_load_dwordx4 v[228:231], v[244:245], off
	v_lshlrev_b32_e32 v240, 8, v250
	v_mov_b32_e32 v241, 0
	v_lshlrev_b64 v[246:247], 10, v[252:253]
	v_lshl_add_u64 v[246:247], vcc, 0, v[246:247]
	v_lshl_add_u64 v[246:247], v[246:247], 0, v[240:241]
	v_lshl_add_u64 v[246:247], v[246:247], 0, v[34:35]
	global_load_dwordx4 v[232:235], v[246:247], off
	global_load_dwordx4 v[236:239], v[246:247], off offset:16
	v_add_u32_e32 v242, v251, v52
	v_mov_b32_e32 v243, 0
	v_lshlrev_b64 v[242:243], 10, v[242:243]
	v_lshl_add_u64 v[242:243], v[242:243], 0, v[240:241]
	v_lshl_add_u64 v[242:243], v[60:61], 0, v[242:243]
	v_mov_b32_e32 v252, 0x2000
	global_load_ushort v190, v[242:243], off
	global_load_ushort v191, v[242:243], off offset:1024
	global_load_ushort v192, v[242:243], off offset:2048
	global_load_ushort v193, v[242:243], off offset:3072
	v_lshl_add_u64 v[242:243], v[242:243], 0, v[252:253]
	global_load_ushort v194, v[242:243], off offset:-4096
	global_load_ushort v195, v[242:243], off offset:-3072
	global_load_ushort v196, v[242:243], off offset:-2048
	global_load_ushort v197, v[242:243], off offset:-1024
	global_load_ushort v198, v[242:243], off
	global_load_ushort v199, v[242:243], off offset:1024
	global_load_ushort v200, v[242:243], off offset:2048
	global_load_ushort v201, v[242:243], off offset:3072
	v_lshl_add_u64 v[242:243], v[242:243], 0, v[252:253]
	global_load_ushort v202, v[242:243], off offset:-4096
	global_load_ushort v203, v[242:243], off offset:-3072
	global_load_ushort v204, v[242:243], off offset:-2048
	global_load_ushort v205, v[242:243], off offset:-1024
	v_lshlrev_b32_e32 v248, 9, v248
	v_lshl_or_b32 v248, v250, 7, v248
	v_lshlrev_b32_e32 v249, 7, v249
	v_add_u32_e32 v252, v248, v54
	v_lshlrev_b64 v[252:253], 12, v[252:253]
	v_or_b32_e32 v252, v252, v249
	v_lshl_add_u64 v[252:253], v[58:59], 0, v[252:253]
	v_add_u32_e32 v250, v248, v70
	v_mov_b32_e32 v251, 0
	v_lshlrev_b64 v[250:251], 12, v[250:251]
	v_or_b32_e32 v250, v250, v249
	v_lshl_add_u64 v[250:251], v[58:59], 0, v[250:251]
	global_load_dwordx4 v[240:243], v[252:253], off
	global_load_dwordx4 v[244:247], v[250:251], off
	v_mov_b32_e32 v255, 1
.LBB0_1100:
	s_mov_b64 s[92:93], 0
	v_readlane_b32 vcc_lo, v254, 28
	v_readlane_b32 vcc_hi, v254, 29
	s_nop 1
	v_or_b32_e32 v252, vcc_lo, v64
	v_mov_b32_e32 v253, vcc_hi
	v_readlane_b32 vcc_lo, v254, 14
	v_readlane_b32 vcc_hi, v254, 15
	v_lshlrev_b64 v[252:253], 10, v[252:253]
	s_nop 0
	v_lshl_add_u64 v[252:253], vcc, 0, v[252:253]
	v_readlane_b32 vcc_lo, v254, 27
	s_mov_b32 vcc_hi, 0
	s_lshl_b32 vcc_lo, vcc_lo, 1
	v_lshl_add_u64 v[252:253], v[252:253], 0, v[80:81]
	s_nop 0
	v_lshl_add_u64 v[252:253], v[252:253], 0, vcc
	global_load_dwordx4 v[96:99], v[68:69], off
	global_load_dwordx4 v[100:103], v[68:69], off offset:64
	global_load_dwordx4 v[104:107], v[68:69], off offset:128
	global_load_dwordx4 v[108:111], v[68:69], off offset:192
	global_load_dwordx2 v[112:113], v[252:253], off
	global_load_dwordx2 v[114:115], v[252:253], off offset:32
	global_load_dwordx2 v[116:117], v[252:253], off offset:64
	global_load_dwordx2 v[118:119], v[252:253], off offset:96
